# ILC6 + nt (streaming) fp8 weight stores in the in-loop converter
# speedup vs baseline: 1.0332x; 1.0150x over previous
; #define LAS __attribute__((address_space(3)))
; __device__ __forceinline__ float clamp8(float x) { return __builtin_amdgcn_fmed3f(x, -448.f, 448.f); }
; __device__ __forceinline__ void cvt_finish(const CvtDesc& d, const float (&t)[64], LAS float* scr, int lane) {
;     ...
;     if (d.f8) {
; #pragma unroll
;         for (int j = 0; j < 8; ++j) { const int n = (lane >> 3) + 8 * j; const LAS float* s = scr + (8 * c) * 65 + n;
;             int a = __builtin_amdgcn_cvt_pk_fp8_f32(clamp8(s[0 * 65] * W8_SCALE), clamp8(s[1 * 65] * W8_SCALE), 0, false); a = __builtin_amdgcn_cvt_pk_fp8_f32(clamp8(s[2 * 65] * W8_SCALE), clamp8(s[3 * 65] * W8_SCALE), a, true);
;             int b = __builtin_amdgcn_cvt_pk_fp8_f32(clamp8(s[4 * 65] * W8_SCALE), clamp8(s[5 * 65] * W8_SCALE), 0, false); b = __builtin_amdgcn_cvt_pk_fp8_f32(clamp8(s[6 * 65] * W8_SCALE), clamp8(s[7 * 65] * W8_SCALE), b, true);
;             __builtin_nontemporal_store((u32x2){(unsigned)a, (unsigned)b}, (u32x2*)(d.dst + (size_t)n * d.dKB + 8 * c)); }
.Lilc_n_da:
	s_cmp_eq_u32 s42, 0
	s_cbranch_scc1 .Lilc_np_da
	s_mov_b32 s53, 4
	v_mul_f32_e32 v232, 0x42800000, v232
	v_mul_f32_e32 v233, 0x42800000, v233
	v_mul_f32_e32 v234, 0x42800000, v234
	v_mul_f32_e32 v235, 0x42800000, v235
	v_mul_f32_e32 v236, 0x42800000, v236
	v_mul_f32_e32 v237, 0x42800000, v237
	v_mul_f32_e32 v238, 0x42800000, v238
	v_mul_f32_e32 v239, 0x42800000, v239
	v_mul_f32_e32 v240, 0x42800000, v240
	v_mul_f32_e32 v241, 0x42800000, v241
	v_mul_f32_e32 v242, 0x42800000, v242
	v_mul_f32_e32 v243, 0x42800000, v243
	v_mul_f32_e32 v244, 0x42800000, v244
	v_mul_f32_e32 v245, 0x42800000, v245
	v_mul_f32_e32 v246, 0x42800000, v246
	v_mul_f32_e32 v247, 0x42800000, v247
	v_mul_f32_e32 v248, 0x42800000, v248
	v_mul_f32_e32 v249, 0x42800000, v249
	v_mul_f32_e32 v250, 0x42800000, v250
	v_mul_f32_e32 v251, 0x42800000, v251
	v_mul_f32_e32 v206, 0x42800000, v206
	v_mul_f32_e32 v207, 0x42800000, v207
	v_mul_f32_e32 v208, 0x42800000, v208
	v_mul_f32_e32 v209, 0x42800000, v209
	v_mul_f32_e32 v210, 0x42800000, v210
	v_mul_f32_e32 v211, 0x42800000, v211
	v_mul_f32_e32 v212, 0x42800000, v212
	v_mul_f32_e32 v213, 0x42800000, v213
	v_mul_f32_e32 v214, 0x42800000, v214
	v_mul_f32_e32 v215, 0x42800000, v215
	v_mul_f32_e32 v216, 0x42800000, v216
	v_mul_f32_e32 v217, 0x42800000, v217
	v_med3_f32 v232, v232, s93, v224
	v_med3_f32 v233, v233, s93, v224
	v_med3_f32 v234, v234, s93, v224
	v_med3_f32 v235, v235, s93, v224
	v_med3_f32 v236, v236, s93, v224
	v_med3_f32 v237, v237, s93, v224
	v_med3_f32 v238, v238, s93, v224
	v_med3_f32 v239, v239, s93, v224
	v_med3_f32 v240, v240, s93, v224
	v_med3_f32 v241, v241, s93, v224
	v_med3_f32 v242, v242, s93, v224
	v_med3_f32 v243, v243, s93, v224
	v_med3_f32 v244, v244, s93, v224
	v_med3_f32 v245, v245, s93, v224
	v_med3_f32 v246, v246, s93, v224
	v_med3_f32 v247, v247, s93, v224
	v_med3_f32 v248, v248, s93, v224
	v_med3_f32 v249, v249, s93, v224
	v_med3_f32 v250, v250, s93, v224
	v_med3_f32 v251, v251, s93, v224
	v_med3_f32 v206, v206, s93, v224
	v_med3_f32 v207, v207, s93, v224
	v_med3_f32 v208, v208, s93, v224
	v_med3_f32 v209, v209, s93, v224
	v_med3_f32 v210, v210, s93, v224
	v_med3_f32 v211, v211, s93, v224
	v_med3_f32 v212, v212, s93, v224
	v_med3_f32 v213, v213, s93, v224
	v_med3_f32 v214, v214, s93, v224
	v_med3_f32 v215, v215, s93, v224
	v_med3_f32 v216, v216, s93, v224
	v_med3_f32 v217, v217, s93, v224
	v_lshlrev_b32_e32 v230, 3, v226
	v_lshl_add_u32 v225, v229, s42, v230
	v_cvt_pk_fp8_f32 v252, v232, v236
	v_cvt_pk_fp8_f32 v253, v248, v206
	v_cvt_pk_fp8_f32 v252, v240, v244 op_sel:[0,0,1]
	v_cvt_pk_fp8_f32 v253, v210, v214 op_sel:[0,0,1]
	s_nop 0
	global_store_dwordx2 v225, v[252:253], s[40:41] nt
	v_add_u32_e32 v225, s43, v225
	v_cvt_pk_fp8_f32 v252, v233, v237
	v_cvt_pk_fp8_f32 v253, v249, v207
	v_cvt_pk_fp8_f32 v252, v241, v245 op_sel:[0,0,1]
	v_cvt_pk_fp8_f32 v253, v211, v215 op_sel:[0,0,1]
	s_nop 0
	global_store_dwordx2 v225, v[252:253], s[40:41] nt
	v_add_u32_e32 v225, s43, v225
	v_cvt_pk_fp8_f32 v252, v234, v238
	v_cvt_pk_fp8_f32 v253, v250, v208
	v_cvt_pk_fp8_f32 v252, v242, v246 op_sel:[0,0,1]
	v_cvt_pk_fp8_f32 v253, v212, v216 op_sel:[0,0,1]
	s_nop 0
	global_store_dwordx2 v225, v[252:253], s[40:41] nt
	v_add_u32_e32 v225, s43, v225
	v_cvt_pk_fp8_f32 v252, v235, v239
	v_cvt_pk_fp8_f32 v253, v251, v209
	v_cvt_pk_fp8_f32 v252, v243, v247 op_sel:[0,0,1]
	v_cvt_pk_fp8_f32 v253, v213, v217 op_sel:[0,0,1]
	s_nop 0
	global_store_dwordx2 v225, v[252:253], s[40:41] nt
	s_mov_b32 s42, 0
	s_branch .Lilc_i_da

; #define LAS __attribute__((address_space(3)))
; __device__ __forceinline__ float clamp8(float x) { return __builtin_amdgcn_fmed3f(x, -448.f, 448.f); }
; __device__ __forceinline__ void cvt_finish(const CvtDesc& d, const float (&t)[64], LAS float* scr, int lane) {
;     ...
;     if (d.f8) {
; #pragma unroll
;         for (int j = 0; j < 8; ++j) { const int n = (lane >> 3) + 8 * j; const LAS float* s = scr + (8 * c) * 65 + n;
;             int a = __builtin_amdgcn_cvt_pk_fp8_f32(clamp8(s[0 * 65] * W8_SCALE), clamp8(s[1 * 65] * W8_SCALE), 0, false); a = __builtin_amdgcn_cvt_pk_fp8_f32(clamp8(s[2 * 65] * W8_SCALE), clamp8(s[3 * 65] * W8_SCALE), a, true);
;             int b = __builtin_amdgcn_cvt_pk_fp8_f32(clamp8(s[4 * 65] * W8_SCALE), clamp8(s[5 * 65] * W8_SCALE), 0, false); b = __builtin_amdgcn_cvt_pk_fp8_f32(clamp8(s[6 * 65] * W8_SCALE), clamp8(s[7 * 65] * W8_SCALE), b, true);
;             __builtin_nontemporal_store((u32x2){(unsigned)a, (unsigned)b}, (u32x2*)(d.dst + (size_t)n * d.dKB + 8 * c)); }
.LBB0_509:
	s_cmp_eq_u32 s42, 0
	s_cbranch_scc1 .Lilc_fd_da
	v_mul_f32_e32 v232, 0x42800000, v232
	v_mul_f32_e32 v233, 0x42800000, v233
	v_mul_f32_e32 v234, 0x42800000, v234
	v_mul_f32_e32 v235, 0x42800000, v235
	v_mul_f32_e32 v236, 0x42800000, v236
	v_mul_f32_e32 v237, 0x42800000, v237
	v_mul_f32_e32 v238, 0x42800000, v238
	v_mul_f32_e32 v239, 0x42800000, v239
	v_mul_f32_e32 v240, 0x42800000, v240
	v_mul_f32_e32 v241, 0x42800000, v241
	v_mul_f32_e32 v242, 0x42800000, v242
	v_mul_f32_e32 v243, 0x42800000, v243
	v_mul_f32_e32 v244, 0x42800000, v244
	v_mul_f32_e32 v245, 0x42800000, v245
	v_mul_f32_e32 v246, 0x42800000, v246
	v_mul_f32_e32 v247, 0x42800000, v247
	v_mul_f32_e32 v248, 0x42800000, v248
	v_mul_f32_e32 v249, 0x42800000, v249
	v_mul_f32_e32 v250, 0x42800000, v250
	v_mul_f32_e32 v251, 0x42800000, v251
	v_mul_f32_e32 v206, 0x42800000, v206
	v_mul_f32_e32 v207, 0x42800000, v207
	v_mul_f32_e32 v208, 0x42800000, v208
	v_mul_f32_e32 v209, 0x42800000, v209
	v_mul_f32_e32 v210, 0x42800000, v210
	v_mul_f32_e32 v211, 0x42800000, v211
	v_mul_f32_e32 v212, 0x42800000, v212
	v_mul_f32_e32 v213, 0x42800000, v213
	v_mul_f32_e32 v214, 0x42800000, v214
	v_mul_f32_e32 v215, 0x42800000, v215
	v_mul_f32_e32 v216, 0x42800000, v216
	v_mul_f32_e32 v217, 0x42800000, v217
	v_med3_f32 v232, v232, s93, v224
	v_med3_f32 v233, v233, s93, v224
	v_med3_f32 v234, v234, s93, v224
	v_med3_f32 v235, v235, s93, v224
	v_med3_f32 v236, v236, s93, v224
	v_med3_f32 v237, v237, s93, v224
	v_med3_f32 v238, v238, s93, v224
	v_med3_f32 v239, v239, s93, v224
	v_med3_f32 v240, v240, s93, v224
	v_med3_f32 v241, v241, s93, v224
	v_med3_f32 v242, v242, s93, v224
	v_med3_f32 v243, v243, s93, v224
	v_med3_f32 v244, v244, s93, v224
	v_med3_f32 v245, v245, s93, v224
	v_med3_f32 v246, v246, s93, v224
	v_med3_f32 v247, v247, s93, v224
	v_med3_f32 v248, v248, s93, v224
	v_med3_f32 v249, v249, s93, v224
	v_med3_f32 v250, v250, s93, v224
	v_med3_f32 v251, v251, s93, v224
	v_med3_f32 v206, v206, s93, v224
	v_med3_f32 v207, v207, s93, v224
	v_med3_f32 v208, v208, s93, v224
	v_med3_f32 v209, v209, s93, v224
	v_med3_f32 v210, v210, s93, v224
	v_med3_f32 v211, v211, s93, v224
	v_med3_f32 v212, v212, s93, v224
	v_med3_f32 v213, v213, s93, v224
	v_med3_f32 v214, v214, s93, v224
	v_med3_f32 v215, v215, s93, v224
	v_med3_f32 v216, v216, s93, v224
	v_med3_f32 v217, v217, s93, v224
	v_lshlrev_b32_e32 v230, 3, v226
	v_lshl_add_u32 v225, v229, s42, v230
	v_cvt_pk_fp8_f32 v252, v232, v236
	v_cvt_pk_fp8_f32 v253, v248, v206
	v_cvt_pk_fp8_f32 v252, v240, v244 op_sel:[0,0,1]
	v_cvt_pk_fp8_f32 v253, v210, v214 op_sel:[0,0,1]
	s_nop 0
	global_store_dwordx2 v225, v[252:253], s[40:41] nt
	v_add_u32_e32 v225, s43, v225
	v_cvt_pk_fp8_f32 v252, v233, v237
	v_cvt_pk_fp8_f32 v253, v249, v207
	v_cvt_pk_fp8_f32 v252, v241, v245 op_sel:[0,0,1]
	v_cvt_pk_fp8_f32 v253, v211, v215 op_sel:[0,0,1]
	s_nop 0
	global_store_dwordx2 v225, v[252:253], s[40:41] nt
	v_add_u32_e32 v225, s43, v225
	v_cvt_pk_fp8_f32 v252, v234, v238
	v_cvt_pk_fp8_f32 v253, v250, v208
	v_cvt_pk_fp8_f32 v252, v242, v246 op_sel:[0,0,1]
	v_cvt_pk_fp8_f32 v253, v212, v216 op_sel:[0,0,1]
	s_nop 0
	global_store_dwordx2 v225, v[252:253], s[40:41] nt
	v_add_u32_e32 v225, s43, v225
	v_cvt_pk_fp8_f32 v252, v235, v239
	v_cvt_pk_fp8_f32 v253, v251, v209
	v_cvt_pk_fp8_f32 v252, v243, v247 op_sel:[0,0,1]
	v_cvt_pk_fp8_f32 v253, v213, v217 op_sel:[0,0,1]
	s_nop 0
	global_store_dwordx2 v225, v[252:253], s[40:41] nt
	s_mov_b32 s42, 0

; #define LAS __attribute__((address_space(3)))
; __device__ __forceinline__ float clamp8(float x) { return __builtin_amdgcn_fmed3f(x, -448.f, 448.f); }
; __device__ __forceinline__ void cvt_finish(const CvtDesc& d, const float (&t)[64], LAS float* scr, int lane) {
;     ...
;     if (d.f8) {
; #pragma unroll
;         for (int j = 0; j < 8; ++j) { const int n = (lane >> 3) + 8 * j; const LAS float* s = scr + (8 * c) * 65 + n;
;             int a = __builtin_amdgcn_cvt_pk_fp8_f32(clamp8(s[0 * 65] * W8_SCALE), clamp8(s[1 * 65] * W8_SCALE), 0, false); a = __builtin_amdgcn_cvt_pk_fp8_f32(clamp8(s[2 * 65] * W8_SCALE), clamp8(s[3 * 65] * W8_SCALE), a, true);
;             int b = __builtin_amdgcn_cvt_pk_fp8_f32(clamp8(s[4 * 65] * W8_SCALE), clamp8(s[5 * 65] * W8_SCALE), 0, false); b = __builtin_amdgcn_cvt_pk_fp8_f32(clamp8(s[6 * 65] * W8_SCALE), clamp8(s[7 * 65] * W8_SCALE), b, true);
;             __builtin_nontemporal_store((u32x2){(unsigned)a, (unsigned)b}, (u32x2*)(d.dst + (size_t)n * d.dKB + 8 * c)); }
.Lilc_p_m:
	s_mov_b32 s53, 4
	v_mul_f32_e32 v232, 0x42800000, v232
	v_mul_f32_e32 v233, 0x42800000, v233
	v_mul_f32_e32 v234, 0x42800000, v234
	v_mul_f32_e32 v235, 0x42800000, v235
	v_mul_f32_e32 v236, 0x42800000, v236
	v_mul_f32_e32 v237, 0x42800000, v237
	v_mul_f32_e32 v238, 0x42800000, v238
	v_mul_f32_e32 v239, 0x42800000, v239
	v_mul_f32_e32 v240, 0x42800000, v240
	v_mul_f32_e32 v241, 0x42800000, v241
	v_mul_f32_e32 v242, 0x42800000, v242
	v_mul_f32_e32 v243, 0x42800000, v243
	v_mul_f32_e32 v244, 0x42800000, v244
	v_mul_f32_e32 v245, 0x42800000, v245
	v_mul_f32_e32 v246, 0x42800000, v246
	v_mul_f32_e32 v247, 0x42800000, v247
	v_mul_f32_e32 v248, 0x42800000, v248
	v_mul_f32_e32 v249, 0x42800000, v249
	v_mul_f32_e32 v250, 0x42800000, v250
	v_mul_f32_e32 v251, 0x42800000, v251
	v_mul_f32_e32 v206, 0x42800000, v206
	v_mul_f32_e32 v207, 0x42800000, v207
	v_mul_f32_e32 v208, 0x42800000, v208
	v_mul_f32_e32 v209, 0x42800000, v209
	v_mul_f32_e32 v210, 0x42800000, v210
	v_mul_f32_e32 v211, 0x42800000, v211
	v_mul_f32_e32 v212, 0x42800000, v212
	v_mul_f32_e32 v213, 0x42800000, v213
	v_mul_f32_e32 v214, 0x42800000, v214
	v_mul_f32_e32 v215, 0x42800000, v215
	v_mul_f32_e32 v216, 0x42800000, v216
	v_mul_f32_e32 v217, 0x42800000, v217
	v_med3_f32 v232, v232, s93, v224
	v_med3_f32 v233, v233, s93, v224
	v_med3_f32 v234, v234, s93, v224
	v_med3_f32 v235, v235, s93, v224
	v_med3_f32 v236, v236, s93, v224
	v_med3_f32 v237, v237, s93, v224
	v_med3_f32 v238, v238, s93, v224
	v_med3_f32 v239, v239, s93, v224
	v_med3_f32 v240, v240, s93, v224
	v_med3_f32 v241, v241, s93, v224
	v_med3_f32 v242, v242, s93, v224
	v_med3_f32 v243, v243, s93, v224
	v_med3_f32 v244, v244, s93, v224
	v_med3_f32 v245, v245, s93, v224
	v_med3_f32 v246, v246, s93, v224
	v_med3_f32 v247, v247, s93, v224
	v_med3_f32 v248, v248, s93, v224
	v_med3_f32 v249, v249, s93, v224
	v_med3_f32 v250, v250, s93, v224
	v_med3_f32 v251, v251, s93, v224
	v_med3_f32 v206, v206, s93, v224
	v_med3_f32 v207, v207, s93, v224
	v_med3_f32 v208, v208, s93, v224
	v_med3_f32 v209, v209, s93, v224
	v_med3_f32 v210, v210, s93, v224
	v_med3_f32 v211, v211, s93, v224
	v_med3_f32 v212, v212, s93, v224
	v_med3_f32 v213, v213, s93, v224
	v_med3_f32 v214, v214, s93, v224
	v_med3_f32 v215, v215, s93, v224
	v_med3_f32 v216, v216, s93, v224
	v_med3_f32 v217, v217, s93, v224
	v_lshlrev_b32_e32 v230, 3, v226
	v_lshl_add_u32 v225, v229, s42, v230
	v_cvt_pk_fp8_f32 v252, v232, v236
	v_cvt_pk_fp8_f32 v253, v248, v206
	v_cvt_pk_fp8_f32 v252, v240, v244 op_sel:[0,0,1]
	v_cvt_pk_fp8_f32 v253, v210, v214 op_sel:[0,0,1]
	s_nop 0
	global_store_dwordx2 v225, v[252:253], s[40:41] nt
	v_add_u32_e32 v225, s43, v225
	v_cvt_pk_fp8_f32 v252, v233, v237
	v_cvt_pk_fp8_f32 v253, v249, v207
	v_cvt_pk_fp8_f32 v252, v241, v245 op_sel:[0,0,1]
	v_cvt_pk_fp8_f32 v253, v211, v215 op_sel:[0,0,1]
	s_nop 0
	global_store_dwordx2 v225, v[252:253], s[40:41] nt
	v_add_u32_e32 v225, s43, v225
	v_cvt_pk_fp8_f32 v252, v234, v238
	v_cvt_pk_fp8_f32 v253, v250, v208
	v_cvt_pk_fp8_f32 v252, v242, v246 op_sel:[0,0,1]
	v_cvt_pk_fp8_f32 v253, v212, v216 op_sel:[0,0,1]
	s_nop 0
	global_store_dwordx2 v225, v[252:253], s[40:41] nt
	v_add_u32_e32 v225, s43, v225
	v_cvt_pk_fp8_f32 v252, v235, v239
	v_cvt_pk_fp8_f32 v253, v251, v209
	v_cvt_pk_fp8_f32 v252, v243, v247 op_sel:[0,0,1]
	v_cvt_pk_fp8_f32 v253, v213, v217 op_sel:[0,0,1]
	s_nop 0
	global_store_dwordx2 v225, v[252:253], s[40:41] nt
	s_mov_b32 s42, 0
	s_branch .Lilc_i_m

; #define LAS __attribute__((address_space(3)))
; __device__ __forceinline__ float clamp8(float x) { return __builtin_amdgcn_fmed3f(x, -448.f, 448.f); }
; #define VM_WAIT() asm volatile("s_waitcnt vmcnt(0)" ::: "memory")
;     ...
;             VM_WAIT();
;             __syncthreads();
;         }
; __device__ __forceinline__ void cvt_finish(const CvtDesc& d, const float (&t)[64], LAS float* scr, int lane) {
;     ...
;     if (d.f8) {
; #pragma unroll
;         for (int j = 0; j < 8; ++j) { const int n = (lane >> 3) + 8 * j; const LAS float* s = scr + (8 * c) * 65 + n;
;             int a = __builtin_amdgcn_cvt_pk_fp8_f32(clamp8(s[0 * 65] * W8_SCALE), clamp8(s[1 * 65] * W8_SCALE), 0, false); a = __builtin_amdgcn_cvt_pk_fp8_f32(clamp8(s[2 * 65] * W8_SCALE), clamp8(s[3 * 65] * W8_SCALE), a, true);
;             int b = __builtin_amdgcn_cvt_pk_fp8_f32(clamp8(s[4 * 65] * W8_SCALE), clamp8(s[5 * 65] * W8_SCALE), 0, false); b = __builtin_amdgcn_cvt_pk_fp8_f32(clamp8(s[6 * 65] * W8_SCALE), clamp8(s[7 * 65] * W8_SCALE), b, true);
;             __builtin_nontemporal_store((u32x2){(unsigned)a, (unsigned)b}, (u32x2*)(d.dst + (size_t)n * d.dKB + 8 * c)); }
.Lilc_wd_m:
	s_cmp_eq_u32 s28, 64
	s_barrier
	v_mfma_f32_32x32x16_bf16 v[48:63], v[70:73], v[86:89], v[48:63]
	v_mfma_f32_32x32x16_bf16 v[48:63], v[74:77], v[90:93], v[48:63]
	v_mfma_f32_32x32x16_bf16 v[48:63], v[78:81], v[174:177], v[48:63]
	s_cbranch_scc0 .LBB0_786
	s_cmp_eq_u32 s42, 0
	s_cbranch_scc1 .Lilc_fd_m
	s_waitcnt vmcnt(0)
	v_mul_f32_e32 v232, 0x42800000, v232
	v_mul_f32_e32 v233, 0x42800000, v233
	v_mul_f32_e32 v234, 0x42800000, v234
	v_mul_f32_e32 v235, 0x42800000, v235
	v_mul_f32_e32 v236, 0x42800000, v236
	v_mul_f32_e32 v237, 0x42800000, v237
	v_mul_f32_e32 v238, 0x42800000, v238
	v_mul_f32_e32 v239, 0x42800000, v239
	v_mul_f32_e32 v240, 0x42800000, v240
	v_mul_f32_e32 v241, 0x42800000, v241
	v_mul_f32_e32 v242, 0x42800000, v242
	v_mul_f32_e32 v243, 0x42800000, v243
	v_mul_f32_e32 v244, 0x42800000, v244
	v_mul_f32_e32 v245, 0x42800000, v245
	v_mul_f32_e32 v246, 0x42800000, v246
	v_mul_f32_e32 v247, 0x42800000, v247
	v_mul_f32_e32 v248, 0x42800000, v248
	v_mul_f32_e32 v249, 0x42800000, v249
	v_mul_f32_e32 v250, 0x42800000, v250
	v_mul_f32_e32 v251, 0x42800000, v251
	v_mul_f32_e32 v206, 0x42800000, v206
	v_mul_f32_e32 v207, 0x42800000, v207
	v_mul_f32_e32 v208, 0x42800000, v208
	v_mul_f32_e32 v209, 0x42800000, v209
	v_mul_f32_e32 v210, 0x42800000, v210
	v_mul_f32_e32 v211, 0x42800000, v211
	v_mul_f32_e32 v212, 0x42800000, v212
	v_mul_f32_e32 v213, 0x42800000, v213
	v_mul_f32_e32 v214, 0x42800000, v214
	v_mul_f32_e32 v215, 0x42800000, v215
	v_mul_f32_e32 v216, 0x42800000, v216
	v_mul_f32_e32 v217, 0x42800000, v217
	v_med3_f32 v232, v232, s93, v224
	v_med3_f32 v233, v233, s93, v224
	v_med3_f32 v234, v234, s93, v224
	v_med3_f32 v235, v235, s93, v224
	v_med3_f32 v236, v236, s93, v224
	v_med3_f32 v237, v237, s93, v224
	v_med3_f32 v238, v238, s93, v224
	v_med3_f32 v239, v239, s93, v224
	v_med3_f32 v240, v240, s93, v224
	v_med3_f32 v241, v241, s93, v224
	v_med3_f32 v242, v242, s93, v224
	v_med3_f32 v243, v243, s93, v224
	v_med3_f32 v244, v244, s93, v224
	v_med3_f32 v245, v245, s93, v224
	v_med3_f32 v246, v246, s93, v224
	v_med3_f32 v247, v247, s93, v224
	v_med3_f32 v248, v248, s93, v224
	v_med3_f32 v249, v249, s93, v224
	v_med3_f32 v250, v250, s93, v224
	v_med3_f32 v251, v251, s93, v224
	v_med3_f32 v206, v206, s93, v224
	v_med3_f32 v207, v207, s93, v224
	v_med3_f32 v208, v208, s93, v224
	v_med3_f32 v209, v209, s93, v224
	v_med3_f32 v210, v210, s93, v224
	v_med3_f32 v211, v211, s93, v224
	v_med3_f32 v212, v212, s93, v224
	v_med3_f32 v213, v213, s93, v224
	v_med3_f32 v214, v214, s93, v224
	v_med3_f32 v215, v215, s93, v224
	v_med3_f32 v216, v216, s93, v224
	v_med3_f32 v217, v217, s93, v224
	v_lshlrev_b32_e32 v230, 3, v226
	v_lshl_add_u32 v225, v229, s42, v230
	v_cvt_pk_fp8_f32 v252, v232, v236
	v_cvt_pk_fp8_f32 v253, v248, v206
	v_cvt_pk_fp8_f32 v252, v240, v244 op_sel:[0,0,1]
	v_cvt_pk_fp8_f32 v253, v210, v214 op_sel:[0,0,1]
	s_nop 0
	global_store_dwordx2 v225, v[252:253], s[40:41] nt
	v_add_u32_e32 v225, s43, v225
	v_cvt_pk_fp8_f32 v252, v233, v237
	v_cvt_pk_fp8_f32 v253, v249, v207
	v_cvt_pk_fp8_f32 v252, v241, v245 op_sel:[0,0,1]
	v_cvt_pk_fp8_f32 v253, v211, v215 op_sel:[0,0,1]
	s_nop 0
	global_store_dwordx2 v225, v[252:253], s[40:41] nt
	v_add_u32_e32 v225, s43, v225
	v_cvt_pk_fp8_f32 v252, v234, v238
	v_cvt_pk_fp8_f32 v253, v250, v208
	v_cvt_pk_fp8_f32 v252, v242, v246 op_sel:[0,0,1]
	v_cvt_pk_fp8_f32 v253, v212, v216 op_sel:[0,0,1]
	s_nop 0
	global_store_dwordx2 v225, v[252:253], s[40:41] nt
	v_add_u32_e32 v225, s43, v225
	v_cvt_pk_fp8_f32 v252, v235, v239
	v_cvt_pk_fp8_f32 v253, v251, v209
	v_cvt_pk_fp8_f32 v252, v243, v247 op_sel:[0,0,1]
	v_cvt_pk_fp8_f32 v253, v213, v217 op_sel:[0,0,1]
	s_nop 0
	global_store_dwordx2 v225, v[252:253], s[40:41] nt
	s_mov_b32 s42, 0
